# v47 + attention: the next block's block-mean key tile is prefetched beside its first K/V/Q loads and written to LDS at the block start
# baseline (speedup 1.0000x reference)
.LBB0_845:
	s_cmp_lt_i32 s92, 9
	s_cselect_b64 s[2:3], -1, 0
	s_and_b64 s[0:1], s[2:3], s[0:1]
	v_writelane_b32 v254, s0, 6
	s_andn2_b64 vcc, exec, s[0:1]
	s_nop 0
	v_writelane_b32 v254, s1, 7
	v_writelane_b32 v254, s85, 8
	v_writelane_b32 v254, s76, 9
	s_nop 1
	v_writelane_b32 v254, s77, 10
	s_cbranch_vccnz .LBB0_1552
	s_mov_b32 s100, 0
	s_abs_i32 s33, s87
	v_cvt_f32_u32_e32 v0, s33
	s_sub_i32 s3, 0, s33
	s_add_i32 s0, s87, 0x1ff
	s_ashr_i32 s2, s0, 31
	v_rcp_iflag_f32_e32 v0, v0
	s_abs_i32 s0, s0
	s_ashr_i32 s40, s87, 31
	s_xor_b32 s2, s2, s40
	v_mul_f32_e32 v0, 0x4f7ffffe, v0
	v_cvt_u32_f32_e32 v0, v0
	s_mul_hi_i32 s1, s90, 0x92492493
	v_readfirstlane_b32 s41, v0
	s_mul_i32 s3, s3, s41
	s_mul_hi_u32 s3, s41, s3
	s_add_i32 s41, s41, s3
	s_mul_hi_u32 s3, s0, s41
	s_mul_i32 s4, s3, s33
	s_sub_i32 s0, s0, s4
	s_add_i32 s5, s3, 1
	s_sub_i32 s4, s0, s33
	s_cmp_ge_u32 s0, s33
	s_cselect_b32 s3, s5, s3
	s_cselect_b32 s0, s4, s0
	s_add_i32 s4, s3, 1
	s_cmp_ge_u32 s0, s33
	s_cselect_b32 s0, s4, s3
	s_xor_b32 s0, s0, s2
	s_sub_i32 s0, s0, s2
	s_mul_i32 s4, s0, s90
	s_add_i32 s0, s4, s0
	s_add_i32 s1, s1, s90
	s_min_i32 s42, s0, 0x200
	s_lshr_b32 s0, s1, 31
	s_ashr_i32 s1, s1, 8
	s_add_i32 s2, s1, s0
	s_mul_i32 s0, s2, 0x1c0
	s_sub_i32 s5, s90, s0
	s_cmpk_lt_i32 s5, 0xe0
	s_cselect_b64 s[0:1], -1, 0
	v_writelane_b32 v254, s0, 11
	s_add_u32 s57, s66, 0x6a00000
	s_addc_u32 s61, s67, 0
	v_writelane_b32 v254, s1, 12
	s_mul_i32 s1, s2, 0x1c00000
	s_mul_hi_i32 s0, s2, 0x1c00000
	s_add_u32 s6, s57, s1
	s_addc_u32 s7, s61, s0
	s_add_u32 s62, s66, 0x580000
	v_writelane_b32 v254, s6, 13
	s_addc_u32 s63, s67, 0
	s_mul_i32 s1, s2, 0xe000
	v_writelane_b32 v254, s7, 14
	s_mul_hi_i32 s0, s2, 0xe000
	s_add_u32 s6, s62, s1
	s_addc_u32 s7, s63, s0
	s_lshl_b32 s0, s89, 7
	s_add_i32 s0, s0, 0
	s_add_i32 s0, s0, 0x22a00
	s_add_u32 s68, s66, 0x380000
	v_writelane_b32 v254, s6, 15
	s_addc_u32 s69, s67, 0
	s_cmpk_lt_i32 s90, 0xe00
	v_writelane_b32 v254, s7, 16
	v_writelane_b32 v254, s0, 17
	s_cselect_b64 s[16:17], -1, 0
	s_add_u32 s0, s66, 0x22a00000
	s_addc_u32 s1, s67, 0
	v_writelane_b32 v254, s0, 18
	s_add_i32 s43, s87, 0xdff
	s_nop 0
	v_writelane_b32 v254, s1, 19
	s_bfe_u32 s0, s5, 0x5001a
	s_add_i32 s3, s5, s0
	s_sext_i32_i16 s0, s3
	s_lshr_b32 s0, s0, 5
	s_bfe_i64 s[0:1], s[0:1], 0x100000
	s_lshl_b64 s[0:1], s[0:1], 22
	v_writelane_b32 v254, s0, 20
	s_nop 1
	v_writelane_b32 v254, s1, 21
	s_and_b32 s0, s3, 0xffe0
	s_sub_i32 s0, s5, s0
	s_sext_i32_i16 s0, s0
	s_lshl_b32 s0, s0, 6
	v_writelane_b32 v254, s5, 22
	s_ashr_i32 s1, s0, 31
	v_writelane_b32 v254, s0, 23
	s_nop 1
	v_writelane_b32 v254, s1, 24
	s_lshl_b32 s0, s89, 3
	v_writelane_b32 v254, s0, 25
	v_writelane_b32 v254, s4, 26
	s_mul_hi_i32 s0, s2, 0x3800000
	v_writelane_b32 v254, s0, 27
	s_mul_i32 s0, s2, 0x3800000
	v_writelane_b32 v254, s0, 28
	s_mul_hi_i32 s1, s2, 0x1c00
	s_mul_i32 s0, s2, 0x1c00
	v_writelane_b32 v254, s0, 29
	s_cmp_gt_i32 s42, s4
	s_nop 0
	v_writelane_b32 v254, s1, 30
	s_mov_b64 s[0:1], -1
	s_cbranch_scc1 .LBB0_1025
	s_abs_i32 s1, s43
	s_mul_hi_u32 s2, s1, s41
	s_mul_i32 s3, s2, s33
	s_ashr_i32 s0, s43, 31
	s_sub_i32 s1, s1, s3
	s_xor_b32 s0, s0, s40
	s_add_i32 s3, s2, 1
	s_sub_i32 s4, s1, s33
	s_cmp_ge_u32 s1, s33
	s_cselect_b32 s2, s3, s2
	s_cselect_b32 s1, s4, s1
	s_add_i32 s3, s2, 1
	s_cmp_ge_u32 s1, s33
	s_cselect_b32 s1, s3, s2
	s_xor_b32 s1, s1, s0
	s_sub_i32 s44, s1, s0
	s_cmp_gt_i32 s44, 0
	s_cselect_b64 s[0:1], -1, 0
	s_and_b64 s[2:3], s[0:1], s[16:17]
	v_cndmask_b32_e64 v0, 0, 1, s[2:3]
	v_cmp_ne_u32_e64 s[0:1], 1, v0
	s_andn2_b64 vcc, exec, s[2:3]
	v_mbcnt_lo_u32_b32 v128, -1, 0
	v_mbcnt_hi_u32_b32 v128, -1, v128
	s_cbranch_vccnz .LBB0_850
	v_readlane_b32 s2, v254, 11
	v_readlane_b32 s3, v254, 12
	s_and_b64 vcc, exec, s[2:3]
	s_cbranch_vccz .LBB0_851
	s_add_i32 s2, 0, 0x23a90
	v_mov_b32_e32 v0, s2
	s_add_i32 s2, 0, 0x23a94
	s_waitcnt lgkmcnt(0)
	v_mov_b32_e32 v1, s2
	ds_read_b32 v0, v0
	ds_read_b32 v1, v1
	s_waitcnt lgkmcnt(0)
	v_readfirstlane_b32 s4, v0
	v_readfirstlane_b32 s5, v1
	s_mov_b32 s6, 0
	s_mov_b32 s46, 1
	s_cbranch_execz .LBB0_852
	s_branch .LBB0_853

.LBB0_1208:
	s_mov_b64 s[88:89], s[66:67]
	v_mbcnt_lo_u32_b32 v48, -1, 0
	v_mbcnt_hi_u32_b32 v48, -1, v48
	s_ashr_i32 s93, s58, 31
	v_add_u32_e32 v0, s79, v48
	v_ashrrev_i32_e32 v16, 4, v0
	v_and_b32_e32 v18, 15, v48
	s_waitcnt vmcnt(0)
	v_mov_b64_e32 v[174:175], v[170:171]
	v_ashrrev_i32_e32 v185, 5, v48
	v_lshlrev_b32_e32 v17, 4, v18
	v_lshlrev_b32_e32 v1, 8, v16
	v_and_b32_e32 v2, 0x70, v0
	s_cmp_eq_u32 s60, 0
	v_mov_b64_e32 v[172:173], v[168:169]
	s_mov_b32 s74, s60
	v_writelane_b32 v255, s61, 3
	v_and_b32_e32 v184, 31, v48
	v_bitop3_b32 v49, v1, v17, v2 bitop3:0xf6
	v_or_b32_e32 v180, v1, v17
	v_lshlrev_b32_e32 v186, 4, v185
	v_lshlrev_b32_e32 v50, 4, v48
	s_mov_b32 s92, s58
	s_cselect_b64 s[4:5], -1, 0
	s_cmp_lg_u32 s60, 0
	s_mov_b64 s[0:1], -1
	s_cbranch_scc0 .LBB0_1212
	s_movk_i32 s0, 0x100
	v_cmp_gt_i32_e32 vcc, s0, v0
	s_and_saveexec_b64 s[0:1], vcc
	s_cbranch_execz .LBB0_1211
	s_lshl_b64 s[2:3], s[92:93], 12
	s_add_u32 s2, s88, s2
	v_add_u32_e32 v0, 0, v49
	s_addc_u32 s3, s89, s3
	v_mov_b32_e32 v181, v129
	v_add_u32_e32 v4, 0x10800, v0
	v_lshl_add_u64 v[0:1], s[2:3], 0, v[180:181]
	v_add_co_u32_e32 v0, vcc, 0x300000, v0
	s_nop 1
	v_addc_co_u32_e32 v1, vcc, 0, v1, vcc
	s_cmp_eq_u32 s100, 0
	s_cbranch_scc1 .Lkm_fresh
	s_waitcnt vmcnt(0)
	ds_write_b128 v4, v[236:239]
	s_branch .Lkm_done
.Lkm_fresh:
	global_load_dwordx4 v[0:3], v[0:1], off
	s_waitcnt vmcnt(0)
	ds_write_b128 v4, v[0:3]
.Lkm_done:
.LBB0_1211:
	s_or_b64 exec, exec, s[0:1]
	s_movk_i32 s1, 0x70
	v_lshlrev_b32_e32 v51, 8, v184
	v_bitop3_b32 v0, v186, v50, s1 bitop3:0x78
	s_add_i32 s0, 0, 0x10800
	v_add_u32_e32 v54, 32, v186
	v_add3_u32 v19, s0, v0, v51
	v_bitop3_b32 v0, v54, v50, s1 bitop3:0x78
	v_add_u32_e32 v53, 64, v186
	v_add3_u32 v24, s0, v0, v51
	v_bitop3_b32 v0, v53, v50, s1 bitop3:0x78
	v_add_u32_e32 v52, 0x60, v186
	v_add3_u32 v25, s0, v0, v51
	v_bitop3_b32 v0, v52, v50, s1 bitop3:0x78
	s_waitcnt lgkmcnt(0)
	s_barrier
	v_add3_u32 v26, s0, v0, v51
	ds_read_b128 v[0:3], v19
	ds_read_b128 v[20:23], v24
	s_waitcnt lgkmcnt(1)
	v_mfma_f32_32x32x16_bf16 v[0:15], v[0:3], v[140:143], 0
	s_cmp_lg_u32 s74, 1
	s_mov_b32 s0, 0xff800000
	s_waitcnt lgkmcnt(0)
	v_mfma_f32_32x32x16_bf16 v[0:15], v[20:23], v[144:147], v[0:15]
	ds_read_b128 v[20:23], v25
	s_waitcnt lgkmcnt(0)
	v_mfma_f32_32x32x16_bf16 v[0:15], v[20:23], v[148:151], v[0:15]
	ds_read_b128 v[20:23], v26
	s_waitcnt lgkmcnt(0)
	v_mfma_f32_32x32x16_bf16 v[0:15], v[20:23], v[152:155], v[0:15]
	ds_read_b128 v[20:23], v19 offset:128
	s_waitcnt lgkmcnt(0)
	v_mfma_f32_32x32x16_bf16 v[0:15], v[20:23], v[156:159], v[0:15]
	ds_read_b128 v[20:23], v24 offset:128
	s_waitcnt lgkmcnt(0)
	v_mfma_f32_32x32x16_bf16 v[0:15], v[20:23], v[160:163], v[0:15]
	ds_read_b128 v[20:23], v25 offset:128
	s_waitcnt lgkmcnt(0)
	v_mfma_f32_32x32x16_bf16 v[0:15], v[20:23], v[164:167], v[0:15]
	ds_read_b128 v[20:23], v26 offset:128
	s_waitcnt lgkmcnt(0)
	v_mfma_f32_32x32x16_bf16 v[0:15], v[20:23], v[172:175], v[0:15]
	s_nop 11
	v_and_b32_e32 v9, 64, v209
	v_xor_b32_e32 v8, 32, v209
	v_add_u32_e32 v9, 64, v9
	v_cmp_lt_i32_e32 vcc, v8, v9
	s_nop 1
	v_cndmask_b32_e32 v8, v209, v8, vcc
	v_lshlrev_b32_e32 v8, 2, v8
	ds_bpermute_b32 v12, v8, v2
	v_cmp_gt_u32_e32 vcc, 32, v48
	ds_bpermute_b32 v9, v8, v0
	s_waitcnt lgkmcnt(1)
	v_cndmask_b32_e32 v13, v12, v2, vcc
	v_cndmask_b32_e32 v2, v2, v12, vcc
	ds_bpermute_b32 v12, v8, v3
	s_waitcnt lgkmcnt(1)
	v_cndmask_b32_e32 v10, v9, v0, vcc
	v_cndmask_b32_e32 v0, v0, v9, vcc
	ds_bpermute_b32 v9, v8, v1
	s_waitcnt lgkmcnt(1)
	v_cndmask_b32_e32 v14, v12, v3, vcc
	v_cndmask_b32_e32 v3, v3, v12, vcc
	ds_bpermute_b32 v12, v8, v4
	s_waitcnt lgkmcnt(1)
	v_cndmask_b32_e32 v11, v1, v9, vcc
	v_cndmask_b32_e32 v1, v9, v1, vcc
	s_waitcnt lgkmcnt(0)
	v_cndmask_b32_e32 v15, v12, v4, vcc
	v_cndmask_b32_e32 v4, v4, v12, vcc
	ds_bpermute_b32 v12, v8, v5
	s_waitcnt lgkmcnt(0)
	v_cndmask_b32_e32 v19, v12, v5, vcc
	v_cndmask_b32_e32 v5, v5, v12, vcc
	ds_bpermute_b32 v12, v8, v6
	ds_bpermute_b32 v8, v8, v7
	s_waitcnt lgkmcnt(1)
	v_cndmask_b32_e32 v20, v12, v6, vcc
	v_cndmask_b32_e32 v6, v6, v12, vcc
	s_waitcnt lgkmcnt(0)
	v_cndmask_b32_e32 v7, v8, v7, vcc
	s_cselect_b64 vcc, -1, 0
	s_cmp_gt_u32 s74, 2
	v_cndmask_b32_e32 v1, v210, v1, vcc
	s_cselect_b64 vcc, -1, 0
	s_cmp_gt_u32 s74, 3
	v_cndmask_b32_e32 v8, v210, v13, vcc
	s_cselect_b64 vcc, -1, 0
	s_cmp_gt_u32 s74, 4
	v_cndmask_b32_e32 v9, v210, v14, vcc
	s_cselect_b64 vcc, -1, 0
	s_cmp_gt_u32 s74, 5
	v_cndmask_b32_e32 v0, v210, v0, vcc
	s_cselect_b64 vcc, -1, 0
	s_cmp_gt_u32 s74, 6
	v_cndmask_b32_e32 v11, v210, v11, vcc
	s_cselect_b64 vcc, -1, 0
	s_cmp_gt_u32 s74, 7
	v_cndmask_b32_e32 v2, v210, v2, vcc
	s_cselect_b64 vcc, -1, 0
	s_cmp_gt_u32 s74, 8
	v_cndmask_b32_e32 v3, v210, v3, vcc
	s_cselect_b64 vcc, -1, 0
	s_cmp_gt_u32 s74, 9
	v_cndmask_b32_e32 v12, v210, v15, vcc
	s_cselect_b64 vcc, -1, 0
	s_cmp_gt_u32 s74, 10
	v_cndmask_b32_e32 v13, v210, v19, vcc
	s_cselect_b64 vcc, -1, 0
	s_cmp_gt_u32 s74, 11
	v_cndmask_b32_e32 v14, v210, v20, vcc
	s_cselect_b64 vcc, -1, 0
	s_cmp_gt_u32 s74, 12
	v_cndmask_b32_e32 v7, v210, v7, vcc
	s_cselect_b64 vcc, -1, 0
	s_cmp_gt_u32 s74, 13
	v_cndmask_b32_e32 v4, v210, v4, vcc
	s_cselect_b64 vcc, -1, 0
	s_cmp_gt_u32 s74, 14
	v_cndmask_b32_e32 v5, v210, v5, vcc
	s_cselect_b64 vcc, -1, 0
	v_cndmask_b32_e32 v6, v210, v6, vcc
	v_cmp_nlg_f32_e32 vcc, s0, v10
	s_nop 1
	v_cndmask_b32_e32 v19, v10, v210, vcc
	v_cmp_gt_f32_e64 s[0:1], v1, v19
	v_cndmask_b32_e64 v15, 0, -1, vcc
	s_nop 0
	v_cndmask_b32_e64 v19, v19, v1, s[0:1]
	v_cndmask_b32_e64 v15, v15, 1, s[0:1]
	v_cmp_gt_f32_e64 s[0:1], v8, v19
	s_nop 1
	v_cndmask_b32_e64 v19, v19, v8, s[0:1]
	v_cndmask_b32_e64 v15, v15, 2, s[0:1]
	v_cmp_gt_f32_e64 s[0:1], v9, v19
	s_nop 1
	v_cndmask_b32_e64 v19, v19, v9, s[0:1]
	v_cndmask_b32_e64 v15, v15, 3, s[0:1]
	v_cmp_gt_f32_e64 s[0:1], v0, v19
	s_nop 1
	v_cndmask_b32_e64 v19, v19, v0, s[0:1]
	v_cndmask_b32_e64 v15, v15, 4, s[0:1]
	v_cmp_gt_f32_e64 s[0:1], v11, v19
	s_nop 1
	v_cndmask_b32_e64 v19, v19, v11, s[0:1]
	v_cndmask_b32_e64 v15, v15, 5, s[0:1]
	v_cmp_gt_f32_e64 s[0:1], v2, v19
	s_nop 1
	v_cndmask_b32_e64 v19, v19, v2, s[0:1]
	v_cndmask_b32_e64 v15, v15, 6, s[0:1]
	v_cmp_gt_f32_e64 s[0:1], v3, v19
	s_nop 1
	v_cndmask_b32_e64 v19, v19, v3, s[0:1]
	v_cndmask_b32_e64 v15, v15, 7, s[0:1]
	v_cmp_gt_f32_e64 s[0:1], v12, v19
	s_nop 1
	v_cndmask_b32_e64 v19, v19, v12, s[0:1]
	v_cndmask_b32_e64 v15, v15, 8, s[0:1]
	v_cmp_gt_f32_e64 s[0:1], v13, v19
	s_nop 1
	v_cndmask_b32_e64 v19, v19, v13, s[0:1]
	v_cndmask_b32_e64 v15, v15, 9, s[0:1]
	v_cmp_gt_f32_e64 s[0:1], v14, v19
	s_nop 1
	v_cndmask_b32_e64 v19, v19, v14, s[0:1]
	v_cndmask_b32_e64 v15, v15, 10, s[0:1]
	v_cmp_gt_f32_e64 s[0:1], v7, v19
	s_nop 1
	v_cndmask_b32_e64 v19, v19, v7, s[0:1]
	v_cndmask_b32_e64 v15, v15, 11, s[0:1]
	v_cmp_gt_f32_e64 s[0:1], v4, v19
	s_nop 1
	v_cndmask_b32_e64 v19, v19, v4, s[0:1]
	v_cndmask_b32_e64 v15, v15, 12, s[0:1]
	v_cmp_gt_f32_e64 s[0:1], v5, v19
	s_nop 1
	v_cndmask_b32_e64 v19, v19, v5, s[0:1]
	v_cndmask_b32_e64 v15, v15, 13, s[0:1]
	v_cmp_ngt_f32_e64 s[0:1], v6, v19
	s_nop 1
	v_cndmask_b32_e64 v15, 14, v15, s[0:1]
	v_lshlrev_b32_e64 v19, v15, 1
	v_cmp_lt_i32_e64 s[0:1], -1, v15
	s_nop 1
	v_cndmask_b32_e64 v15, 0, v19, s[0:1]
	v_and_b32_e32 v19, 1, v15
	v_cmp_eq_u32_e64 s[0:1], 1, v19
	s_or_b64 s[0:1], vcc, s[0:1]
	v_and_b32_e32 v21, 2, v15
	v_cndmask_b32_e64 v20, v10, v210, s[0:1]
	v_cndmask_b32_e64 v19, 0, -1, s[0:1]
	v_cmp_eq_u32_e64 s[0:1], 0, v21
	v_cmp_gt_f32_e64 s[2:3], v1, v20
	s_and_b64 s[0:1], s[0:1], s[2:3]
	v_cndmask_b32_e64 v20, v20, v1, s[0:1]
	v_and_b32_e32 v21, 4, v15
	v_cndmask_b32_e64 v19, v19, 1, s[0:1]
	v_cmp_eq_u32_e64 s[0:1], 0, v21
	v_cmp_gt_f32_e64 s[2:3], v8, v20
	s_and_b64 s[0:1], s[0:1], s[2:3]
	v_cndmask_b32_e64 v20, v20, v8, s[0:1]
	v_and_b32_e32 v21, 8, v15
	v_cndmask_b32_e64 v19, v19, 2, s[0:1]
	v_cmp_eq_u32_e64 s[0:1], 0, v21
	v_cmp_gt_f32_e64 s[2:3], v9, v20
	s_and_b64 s[0:1], s[0:1], s[2:3]
	v_cndmask_b32_e64 v20, v20, v9, s[0:1]
	v_and_b32_e32 v21, 16, v15
	v_cndmask_b32_e64 v19, v19, 3, s[0:1]
	v_cmp_eq_u32_e64 s[0:1], 0, v21
	v_cmp_gt_f32_e64 s[2:3], v0, v20
	s_and_b64 s[0:1], s[0:1], s[2:3]
	v_cndmask_b32_e64 v20, v20, v0, s[0:1]
	v_and_b32_e32 v21, 32, v15
	v_cndmask_b32_e64 v19, v19, 4, s[0:1]
	v_cmp_eq_u32_e64 s[0:1], 0, v21
	v_cmp_gt_f32_e64 s[2:3], v11, v20
	s_and_b64 s[0:1], s[0:1], s[2:3]
	v_cndmask_b32_e64 v20, v20, v11, s[0:1]
	v_and_b32_e32 v21, 64, v15
	v_cndmask_b32_e64 v19, v19, 5, s[0:1]
	v_cmp_eq_u32_e64 s[0:1], 0, v21
	v_cmp_gt_f32_e64 s[2:3], v2, v20
	s_and_b64 s[0:1], s[0:1], s[2:3]
	v_cndmask_b32_e64 v20, v20, v2, s[0:1]
	v_and_b32_e32 v21, 0x80, v15
	v_cndmask_b32_e64 v19, v19, 6, s[0:1]
	v_cmp_eq_u32_e64 s[0:1], 0, v21
	v_cmp_gt_f32_e64 s[2:3], v3, v20
	s_and_b64 s[0:1], s[0:1], s[2:3]
	v_cndmask_b32_e64 v20, v20, v3, s[0:1]
	v_and_b32_e32 v21, 0x100, v15
	v_cndmask_b32_e64 v19, v19, 7, s[0:1]
	v_cmp_eq_u32_e64 s[0:1], 0, v21
	v_cmp_gt_f32_e64 s[2:3], v12, v20
	s_and_b64 s[0:1], s[0:1], s[2:3]
	v_cndmask_b32_e64 v20, v20, v12, s[0:1]
	v_and_b32_e32 v21, 0x200, v15
	v_cndmask_b32_e64 v19, v19, 8, s[0:1]
	v_cmp_eq_u32_e64 s[0:1], 0, v21
	v_cmp_gt_f32_e64 s[2:3], v13, v20
	s_and_b64 s[0:1], s[0:1], s[2:3]
	v_cndmask_b32_e64 v20, v20, v13, s[0:1]
	v_and_b32_e32 v21, 0x400, v15
	v_cndmask_b32_e64 v19, v19, 9, s[0:1]
	v_cmp_eq_u32_e64 s[0:1], 0, v21
	v_cmp_gt_f32_e64 s[2:3], v14, v20
	s_and_b64 s[0:1], s[0:1], s[2:3]
	v_cndmask_b32_e64 v20, v20, v14, s[0:1]
	v_and_b32_e32 v21, 0x800, v15
	v_cndmask_b32_e64 v19, v19, 10, s[0:1]
	v_cmp_eq_u32_e64 s[0:1], 0, v21
	v_cmp_gt_f32_e64 s[2:3], v7, v20
	s_and_b64 s[0:1], s[0:1], s[2:3]
	v_cndmask_b32_e64 v20, v20, v7, s[0:1]
	v_and_b32_e32 v21, 0x1000, v15
	v_cndmask_b32_e64 v19, v19, 11, s[0:1]
	v_cmp_eq_u32_e64 s[0:1], 0, v21
	v_cmp_gt_f32_e64 s[2:3], v4, v20
	s_and_b64 s[0:1], s[0:1], s[2:3]
	v_cndmask_b32_e64 v20, v20, v4, s[0:1]
	v_and_b32_e32 v21, 0x2000, v15
	v_cndmask_b32_e64 v19, v19, 12, s[0:1]
	v_cmp_eq_u32_e64 s[0:1], 0, v21
	v_cmp_gt_f32_e64 s[2:3], v5, v20
	s_and_b64 s[0:1], s[0:1], s[2:3]
	v_cndmask_b32_e64 v20, v20, v5, s[0:1]
	v_and_b32_e32 v21, 0x4000, v15
	v_cndmask_b32_e64 v19, v19, 13, s[0:1]
	v_cmp_eq_u32_e64 s[0:1], 0, v21
	v_cmp_gt_f32_e64 s[2:3], v6, v20
	s_and_b64 s[0:1], s[0:1], s[2:3]
	v_cndmask_b32_e64 v19, v19, 14, s[0:1]
	v_lshlrev_b32_e64 v20, v19, 1
	v_cmp_lt_i32_e64 s[0:1], -1, v19
	s_nop 1
	v_cndmask_b32_e64 v19, 0, v20, s[0:1]
	v_or_b32_e32 v15, v19, v15
	v_and_b32_e32 v19, 1, v15
	v_cmp_eq_u32_e64 s[0:1], 1, v19
	s_or_b64 vcc, vcc, s[0:1]
	v_cndmask_b32_e32 v10, v10, v210, vcc
	v_and_b32_e32 v20, 2, v15
	v_cndmask_b32_e64 v19, 0, -1, vcc
	v_cmp_eq_u32_e32 vcc, 0, v20
	v_cmp_gt_f32_e64 s[0:1], v1, v10
	s_and_b64 vcc, vcc, s[0:1]
	v_cndmask_b32_e32 v1, v10, v1, vcc
	v_and_b32_e32 v10, 4, v15
	v_cndmask_b32_e64 v19, v19, 1, vcc
	v_cmp_eq_u32_e32 vcc, 0, v10
	v_cmp_gt_f32_e64 s[0:1], v8, v1
	s_and_b64 vcc, vcc, s[0:1]
	v_cndmask_b32_e32 v1, v1, v8, vcc
	v_and_b32_e32 v8, 8, v15
	v_cndmask_b32_e64 v10, v19, 2, vcc
	v_cmp_eq_u32_e32 vcc, 0, v8
	v_cmp_gt_f32_e64 s[0:1], v9, v1
	s_and_b64 vcc, vcc, s[0:1]
	v_cndmask_b32_e32 v1, v1, v9, vcc
	v_and_b32_e32 v9, 16, v15
	v_cndmask_b32_e64 v8, v10, 3, vcc
	v_cmp_eq_u32_e32 vcc, 0, v9
	v_cmp_gt_f32_e64 s[0:1], v0, v1
	s_and_b64 vcc, vcc, s[0:1]
	v_cndmask_b32_e32 v0, v1, v0, vcc
	v_and_b32_e32 v1, 32, v15
	v_cndmask_b32_e64 v8, v8, 4, vcc
	v_cmp_eq_u32_e32 vcc, 0, v1
	v_cmp_gt_f32_e64 s[0:1], v11, v0
	s_and_b64 vcc, vcc, s[0:1]
	v_cndmask_b32_e64 v1, v8, 5, vcc
	v_cndmask_b32_e32 v0, v0, v11, vcc
	v_and_b32_e32 v8, 64, v15
	v_cmp_eq_u32_e32 vcc, 0, v8
	v_cmp_gt_f32_e64 s[0:1], v2, v0
	s_and_b64 vcc, vcc, s[0:1]
	v_cndmask_b32_e32 v0, v0, v2, vcc
	v_and_b32_e32 v2, 0x80, v15
	v_cndmask_b32_e64 v1, v1, 6, vcc
	v_cmp_eq_u32_e32 vcc, 0, v2
	v_cmp_gt_f32_e64 s[0:1], v3, v0
	s_and_b64 vcc, vcc, s[0:1]
	v_cndmask_b32_e32 v0, v0, v3, vcc
	v_and_b32_e32 v2, 0x100, v15
	v_cndmask_b32_e64 v1, v1, 7, vcc
	v_cmp_eq_u32_e32 vcc, 0, v2
	v_cmp_gt_f32_e64 s[0:1], v12, v0
	s_and_b64 vcc, vcc, s[0:1]
	v_cndmask_b32_e32 v0, v0, v12, vcc
	v_and_b32_e32 v2, 0x200, v15
	v_cndmask_b32_e64 v1, v1, 8, vcc
	v_cmp_eq_u32_e32 vcc, 0, v2
	v_cmp_gt_f32_e64 s[0:1], v13, v0
	s_and_b64 vcc, vcc, s[0:1]
	v_cndmask_b32_e32 v0, v0, v13, vcc
	v_and_b32_e32 v2, 0x400, v15
	v_cndmask_b32_e64 v1, v1, 9, vcc
	v_cmp_eq_u32_e32 vcc, 0, v2
	v_cmp_gt_f32_e64 s[0:1], v14, v0
	s_and_b64 vcc, vcc, s[0:1]
	v_cndmask_b32_e32 v0, v0, v14, vcc
	v_and_b32_e32 v2, 0x800, v15
	v_cndmask_b32_e64 v1, v1, 10, vcc
	v_cmp_eq_u32_e32 vcc, 0, v2
	v_cmp_gt_f32_e64 s[0:1], v7, v0
	s_and_b64 vcc, vcc, s[0:1]
	v_cndmask_b32_e32 v0, v0, v7, vcc
	v_and_b32_e32 v2, 0x1000, v15
	v_cndmask_b32_e64 v1, v1, 11, vcc
	v_cmp_eq_u32_e32 vcc, 0, v2
	v_cmp_gt_f32_e64 s[0:1], v4, v0
	s_and_b64 vcc, vcc, s[0:1]
	v_cndmask_b32_e32 v0, v0, v4, vcc
	v_and_b32_e32 v2, 0x2000, v15
	v_cndmask_b32_e64 v1, v1, 12, vcc
	v_cmp_eq_u32_e32 vcc, 0, v2
	v_cmp_gt_f32_e64 s[0:1], v5, v0
	s_and_b64 vcc, vcc, s[0:1]
	v_cndmask_b32_e32 v0, v0, v5, vcc
	v_and_b32_e32 v2, 0x4000, v15
	v_cndmask_b32_e64 v1, v1, 13, vcc
	v_cmp_eq_u32_e32 vcc, 0, v2
	v_cmp_gt_f32_e64 s[0:1], v6, v0
	s_and_b64 s[0:1], vcc, s[0:1]
	s_nop 0
	v_cndmask_b32_e64 v0, v1, 14, s[0:1]
	v_lshlrev_b32_e64 v1, v0, 1
	v_cmp_lt_i32_e32 vcc, -1, v0
	s_mov_b64 s[0:1], 0
	s_nop 0
	v_cndmask_b32_e32 v0, 0, v1, vcc
	v_or_b32_e32 v193, v0, v15

.LBB0_1237:
	v_readlane_b32 s2, v255, 3
	s_add_i32 s61, s2, 1
	v_readlane_b32 s62, v255, 1
	s_cmp_lt_u32 s61, s62
	s_cselect_b32 s2, s61, s2
	s_lshr_b32 s3, s2, 1
	v_readlane_b32 s4, v254, 26
	s_add_i32 s3, s3, s4
	s_ashr_i32 s58, s3, 3
	s_and_b32 s3, s3, 7
	s_and_b32 s2, s2, 1
	s_xor_b32 s4, s3, 15
	s_cmp_eq_u32 s2, 0
	s_cselect_b32 s60, s3, s4
	v_lshl_add_u32 v131, v194, 8, v186
	ds_read_b128 v[96:99], v195 offset:49152
	ds_read_b128 v[112:115], v195 offset:49280
	ds_read_b128 v[116:119], v196 offset:49152
	ds_read_b128 v[120:123], v196 offset:49280
	s_waitcnt lgkmcnt(3)
	v_mfma_f32_32x32x16_bf16 v[96:111], v[96:99], v[140:143], 0
	s_waitcnt lgkmcnt(1)
	v_mfma_f32_32x32x16_bf16 v[96:111], v[116:119], v[144:147], v[96:111]
	ds_read_b128 v[116:119], v197 offset:49152
	ds_read_b128 v[124:127], v197 offset:49280
	s_waitcnt lgkmcnt(1)
	v_mfma_f32_32x32x16_bf16 v[96:111], v[116:119], v[148:151], v[96:111]
	ds_read_b128 v[116:119], v198 offset:49152
	s_waitcnt vmcnt(2)
	ds_read_b128 v[132:135], v198 offset:49280
	s_waitcnt lgkmcnt(1)
	v_mfma_f32_32x32x16_bf16 v[96:111], v[116:119], v[152:155], v[96:111]
	v_mfma_f32_32x32x16_bf16 v[96:111], v[112:115], v[156:159], v[96:111]
	ds_read_b128 v[112:115], v195 offset:57344
	s_waitcnt vmcnt(1)
	ds_read_b128 v[168:171], v195 offset:57472
	ds_read_b128 v[204:207], v196 offset:57344
	ds_read_b128 v[214:217], v196 offset:57472
	ds_read_b128 v[218:221], v197 offset:57344
	ds_read_b128 v[194:197], v197 offset:57472
	ds_read_b128 v[222:225], v198 offset:57344
	ds_read_b128 v[198:201], v198 offset:57472
	v_mfma_f32_32x32x16_bf16 v[96:111], v[120:123], v[160:163], v[96:111]
	v_mfma_f32_32x32x16_bf16 v[96:111], v[124:127], v[164:167], v[96:111]
	s_waitcnt lgkmcnt(8)
	v_mfma_f32_32x32x16_bf16 v[96:111], v[132:135], v[172:175], v[96:111]
	s_ashr_i32 s59, s58, 31
	s_lshl_b64 s[2:3], s[58:59], 20
	s_add_u32 s4, s93, s2
	s_addc_u32 s5, s71, s3
	s_add_u32 s6, s79, s2
	s_addc_u32 s7, s70, s3
	s_lshl_b32 s98, s58, 12
	s_add_u32 s98, s88, s98
	s_addc_u32 s99, s89, 0
	s_add_u32 s98, s98, 0x300000
	s_addc_u32 s99, s99, 0
	global_load_dwordx4 v[236:239], v180, s[98:99]
	s_mov_b32 s100, 1
	v_lshl_add_u64 v[116:117], s[4:5], 0, v[180:181]
	v_lshl_add_u64 v[118:119], s[4:5], 0, v[128:129]
	global_load_dwordx4 v[132:135], v[116:117], off
	global_load_dwordx4 v[136:139], v[118:119], off
	v_lshl_add_u64 v[116:117], s[6:7], 0, v[180:181]
	v_lshl_add_u64 v[118:119], s[6:7], 0, v[128:129]
	global_load_dwordx4 v[176:179], v[116:117], off
	global_load_dwordx4 v[180:183], v[118:119], off
	s_waitcnt lgkmcnt(7)
	v_mfma_f32_32x32x16_bf16 v[112:127], v[112:115], v[140:143], 0
	s_lshl_b32 s4, s60, 16
	s_add_u32 s2, s88, s2
	s_addc_u32 s3, s89, s3
	s_add_u32 s2, s2, s4
	s_addc_u32 s3, s3, 0
	s_add_u32 s2, s2, 0x5ca00000
	s_addc_u32 s3, s3, 0
	s_waitcnt lgkmcnt(5)
	v_mfma_f32_32x32x16_bf16 v[112:127], v[204:207], v[144:147], v[112:127]
	v_add_u32_e32 v128, 32, v131
	global_load_dwordx4 v[140:143], v131, s[2:3]
	global_load_dwordx4 v[144:147], v128, s[2:3]
	v_add_u32_e32 v128, 0x80, v131
	s_waitcnt lgkmcnt(3)
	v_mfma_f32_32x32x16_bf16 v[112:127], v[218:221], v[148:151], v[112:127]
	v_add_u32_e32 v148, 64, v131
	s_waitcnt lgkmcnt(1)
	v_mfma_f32_32x32x16_bf16 v[112:127], v[222:225], v[152:155], v[112:127]
	v_add_u32_e32 v152, 0x60, v131
	global_load_dwordx4 v[148:151], v148, s[2:3]
	s_nop 0
	global_load_dwordx4 v[152:155], v152, s[2:3]
	v_mfma_f32_32x32x16_bf16 v[112:127], v[168:171], v[156:159], v[112:127]
	v_add_u32_e32 v168, 0xc0, v131
	v_mfma_f32_32x32x16_bf16 v[112:127], v[214:217], v[160:163], v[112:127]
	v_add_u32_e32 v160, 0xa0, v131
	v_add_u32_e32 v131, 0xe0, v131
	global_load_dwordx4 v[156:159], v128, s[2:3]
	s_nop 0
	global_load_dwordx4 v[160:163], v160, s[2:3]
	v_mfma_f32_32x32x16_bf16 v[112:127], v[194:197], v[164:167], v[112:127]
	global_load_dwordx4 v[164:167], v168, s[2:3]
	s_nop 0
	global_load_dwordx4 v[168:171], v131, s[2:3]
	s_waitcnt lgkmcnt(0)
	v_mfma_f32_32x32x16_bf16 v[112:127], v[198:201], v[172:175], v[112:127]
	v_exp_f32_e32 v128, v80
	v_add_f32_e32 v80, 0, v64
	v_add_f32_e32 v80, v65, v80
	v_add_f32_e32 v80, v66, v80
	v_add_f32_e32 v80, v67, v80
	v_add_f32_e32 v80, v68, v80
	v_add_f32_e32 v80, v69, v80
	v_add_f32_e32 v80, v70, v80
	v_add_f32_e32 v80, v71, v80
	v_add_f32_e32 v80, v72, v80
	v_add_f32_e32 v80, v73, v80
	v_add_f32_e32 v80, v74, v80
	v_add_f32_e32 v80, v75, v80
	v_add_f32_e32 v80, v76, v80
	v_exp_f32_e32 v131, v81
	v_add_f32_e32 v80, v77, v80
	v_exp_f32_e32 v82, v82
	v_add_f32_e32 v80, v78, v80
	v_exp_f32_e32 v83, v83
	v_add_f32_e32 v80, v79, v80
	v_exp_f32_e32 v84, v84
	v_add_f32_e32 v80, v128, v80
	v_exp_f32_e32 v85, v85
	v_add_f32_e32 v80, v131, v80
	v_exp_f32_e32 v86, v86
	v_add_f32_e32 v80, v82, v80
	v_exp_f32_e32 v87, v87
	v_add_f32_e32 v80, v83, v80
	v_exp_f32_e32 v88, v88
	v_add_f32_e32 v80, v84, v80
	v_exp_f32_e32 v89, v89
	v_add_f32_e32 v80, v85, v80
	v_exp_f32_e32 v90, v90
	v_add_f32_e32 v80, v86, v80
	v_exp_f32_e32 v91, v91
	v_add_f32_e32 v80, v87, v80
	v_exp_f32_e32 v92, v92
	v_add_f32_e32 v80, v88, v80
	v_exp_f32_e32 v93, v93
	v_add_f32_e32 v80, v89, v80
	v_exp_f32_e32 v94, v94
	v_add_f32_e32 v80, v90, v80
	v_exp_f32_e32 v95, v95
	v_add_f32_e32 v80, v91, v80
	v_add_f32_e32 v80, v92, v80
	v_add_f32_e32 v80, v93, v80
	v_add_f32_e32 v80, v94, v80
	v_add_f32_e32 v80, v95, v80
	v_mov_b32_e32 v81, v80
	s_nop 1
	v_permlane32_swap_b32_e32 v80, v81
	v_cvt_pk_bf16_f32 v64, v64, v65
	v_cvt_pk_bf16_f32 v65, v66, v67
	v_cvt_pk_bf16_f32 v66, v68, v69
	v_cvt_pk_bf16_f32 v67, v70, v71
	v_cvt_pk_bf16_f32 v68, v72, v73
	v_cvt_pk_bf16_f32 v69, v74, v75
	v_cvt_pk_bf16_f32 v70, v76, v77
	v_cvt_pk_bf16_f32 v71, v78, v79
	v_cvt_pk_bf16_f32 v72, v128, v131
	v_cvt_pk_bf16_f32 v73, v82, v83
	v_cvt_pk_bf16_f32 v74, v84, v85
	v_cvt_pk_bf16_f32 v75, v86, v87
	v_cvt_pk_bf16_f32 v76, v88, v89
	v_cvt_pk_bf16_f32 v77, v90, v91
	v_cvt_pk_bf16_f32 v78, v92, v93
	v_cvt_pk_bf16_f32 v79, v94, v95
	s_nop 0
	v_permlane32_swap_b32_e32 v64, v66
	v_permlane32_swap_b32_e32 v65, v67
	v_permlane32_swap_b32_e32 v68, v70
	v_permlane32_swap_b32_e32 v69, v71
	v_permlane32_swap_b32_e32 v72, v74
	v_permlane32_swap_b32_e32 v73, v75
	v_permlane32_swap_b32_e32 v76, v78
	v_permlane32_swap_b32_e32 v77, v79
	ds_read_b64_tr_b16 v[82:83], v187 offset:0
	ds_read_b64_tr_b16 v[84:85], v187 offset:0x800
	ds_read_b64_tr_b16 v[86:87], v187 offset:0x1000
	ds_read_b64_tr_b16 v[88:89], v187 offset:0x1800
	ds_read_b64_tr_b16 v[90:91], v187 offset:0x2000
	ds_read_b64_tr_b16 v[92:93], v187 offset:0x2800
	ds_read_b64_tr_b16 v[172:173], v187 offset:0x3000
	ds_read_b64_tr_b16 v[174:175], v187 offset:0x3800
	s_waitcnt lgkmcnt(0)
	ds_read_b64_tr_b16 v[194:195], v187 offset:0x200
	ds_read_b64_tr_b16 v[196:197], v187 offset:0xa00
	ds_read_b64_tr_b16 v[198:199], v187 offset:0x1200
	ds_read_b64_tr_b16 v[200:201], v187 offset:0x1a00
	ds_read_b64_tr_b16 v[204:205], v187 offset:0x2200
	ds_read_b64_tr_b16 v[206:207], v187 offset:0x2a00
	ds_read_b64_tr_b16 v[214:215], v187 offset:0x3200
	ds_read_b64_tr_b16 v[216:217], v187 offset:0x3a00
	s_nop 0
	v_mfma_f32_32x32x16_bf16 v[32:47], v[64:67], v[82:85], v[32:47]
	v_mfma_f32_32x32x16_bf16 v[32:47], v[68:71], v[86:89], v[32:47]
	v_mfma_f32_32x32x16_bf16 v[32:47], v[72:75], v[90:93], v[32:47]
	v_mfma_f32_32x32x16_bf16 v[32:47], v[76:79], v[172:175], v[32:47]
	s_waitcnt lgkmcnt(0)
	ds_read_b64_tr_b16 v[82:83], v187 offset:0x400
	ds_read_b64_tr_b16 v[84:85], v187 offset:0xc00
	ds_read_b64_tr_b16 v[86:87], v187 offset:0x1400
	ds_read_b64_tr_b16 v[88:89], v187 offset:0x1c00
	ds_read_b64_tr_b16 v[90:91], v187 offset:0x2400
	ds_read_b64_tr_b16 v[92:93], v187 offset:0x2c00
	ds_read_b64_tr_b16 v[172:173], v187 offset:0x3400
	ds_read_b64_tr_b16 v[174:175], v187 offset:0x3c00
	v_mfma_f32_32x32x16_bf16 v[48:63], v[64:67], v[194:197], v[48:63]
	v_mfma_f32_32x32x16_bf16 v[48:63], v[68:71], v[198:201], v[48:63]
	v_mfma_f32_32x32x16_bf16 v[48:63], v[72:75], v[204:207], v[48:63]
	v_mfma_f32_32x32x16_bf16 v[48:63], v[76:79], v[214:217], v[48:63]
	s_waitcnt lgkmcnt(0)
	ds_read_b64_tr_b16 v[194:195], v187 offset:0x600
	ds_read_b64_tr_b16 v[196:197], v187 offset:0xe00
	ds_read_b64_tr_b16 v[198:199], v187 offset:0x1600
	ds_read_b64_tr_b16 v[200:201], v187 offset:0x1e00
	ds_read_b64_tr_b16 v[204:205], v187 offset:0x2600
	ds_read_b64_tr_b16 v[206:207], v187 offset:0x2e00
	ds_read_b64_tr_b16 v[214:215], v187 offset:0x3600
	ds_read_b64_tr_b16 v[216:217], v187 offset:0x3e00
	v_mfma_f32_32x32x16_bf16 v[16:31], v[64:67], v[82:85], v[16:31]
	v_mfma_f32_32x32x16_bf16 v[16:31], v[68:71], v[86:89], v[16:31]
	v_mfma_f32_32x32x16_bf16 v[16:31], v[72:75], v[90:93], v[16:31]
	v_mfma_f32_32x32x16_bf16 v[16:31], v[76:79], v[172:175], v[16:31]
	s_waitcnt lgkmcnt(0)
	v_mfma_f32_32x32x16_bf16 v[0:15], v[64:67], v[194:197], v[0:15]
	v_readlane_b32 s2, v254, 44
	v_readlane_b32 s3, v254, 45
	s_andn2_b64 vcc, exec, s[2:3]
	v_mfma_f32_32x32x16_bf16 v[0:15], v[68:71], v[198:201], v[0:15]
	v_mfma_f32_32x32x16_bf16 v[0:15], v[72:75], v[204:207], v[0:15]
	v_mfma_f32_32x32x16_bf16 v[0:15], v[76:79], v[214:217], v[0:15]
	s_cbranch_vccnz .LBB0_1239
	s_movk_i32 s54, 0xda
	s_movk_i32 s56, 0xdb
	v_cmp_gt_i32_e64 s[54:55], s54, v192
	v_cmp_gt_i32_e64 s[56:57], s56, v192
	s_and_b64 s[54:55], s[56:57], s[54:55]
	s_movk_i32 s24, 0xd8
	v_cndmask_b32_e64 v111, v111, v210, s[56:57]
	s_movk_i32 s56, 0xd9
	v_cmp_gt_i32_e64 s[56:57], s56, v192
	s_movk_i32 s22, 0xd3
	v_cmp_gt_i32_e64 s[52:53], s24, v192
	v_cndmask_b32_e64 v110, v110, v210, s[54:55]
	s_and_b64 s[54:55], s[54:55], s[56:57]
	s_movk_i32 s20, 0xd2
	v_cmp_gt_i32_e64 s[50:51], s22, v192
	s_and_b64 s[52:53], s[54:55], s[52:53]
	s_movk_i32 s18, 0xd1
	v_cmp_gt_i32_e64 s[48:49], s20, v192
	s_and_b64 s[50:51], s[52:53], s[50:51]
	s_movk_i32 s16, 0xd0
	v_cmp_gt_i32_e64 s[46:47], s18, v192
	s_and_b64 s[48:49], s[50:51], s[48:49]
	s_movk_i32 s14, 0xcb
	v_cmp_gt_i32_e64 s[44:45], s16, v192
	s_and_b64 s[46:47], s[48:49], s[46:47]
	s_movk_i32 s12, 0xca
	v_cmp_gt_i32_e64 s[42:43], s14, v192
	s_and_b64 s[44:45], s[46:47], s[44:45]
	s_movk_i32 s10, 0xc9
	v_cmp_gt_i32_e64 s[40:41], s12, v192
	s_and_b64 s[42:43], s[44:45], s[42:43]
	s_movk_i32 s8, 0xc8
	v_cmp_gt_i32_e64 s[38:39], s10, v192
	s_and_b64 s[40:41], s[42:43], s[40:41]
	s_movk_i32 s2, 0xc0
	s_movk_i32 s6, 0xc3
	v_cmp_gt_i32_e64 s[36:37], s8, v192
	s_and_b64 s[38:39], s[40:41], s[38:39]
	v_cmp_gt_i32_e64 s[26:27], s2, v192
	s_movk_i32 s2, 0xe0
	s_movk_i32 s4, 0xc2
	v_cmp_gt_i32_e64 s[34:35], s6, v192
	s_and_b64 s[36:37], s[38:39], s[36:37]
	v_cmp_gt_i32_e32 vcc, s2, v192
	s_movk_i32 s2, 0xc1
	v_cmp_gt_i32_e64 s[30:31], s4, v192
	s_and_b64 s[34:35], s[36:37], s[34:35]
	v_cmp_gt_i32_e64 s[28:29], s2, v192
	s_and_b64 s[30:31], s[34:35], s[30:31]
	s_and_b64 s[28:29], s[30:31], s[28:29]
	s_and_b64 s[26:27], s[28:29], s[26:27]
	v_cndmask_b32_e64 v109, v109, v210, s[54:55]
	s_movk_i32 s54, 0xfa
	v_cndmask_b32_e64 v96, v96, v210, s[26:27]
	s_movk_i32 s26, 0xfb
	s_movk_i32 s56, 0xf9
	v_cmp_gt_i32_e64 s[54:55], s54, v192
	v_cmp_gt_i32_e64 s[26:27], s26, v192
	s_movk_i32 s24, 0xf8
	v_cmp_gt_i32_e64 s[56:57], s56, v192
	v_cndmask_b32_e64 v127, v127, v210, s[26:27]
	s_and_b64 s[26:27], s[26:27], s[54:55]
	s_movk_i32 s22, 0xf3
	v_cmp_gt_i32_e64 s[24:25], s24, v192
	v_cndmask_b32_e64 v126, v126, v210, s[26:27]
	s_and_b64 s[26:27], s[26:27], s[56:57]
	s_movk_i32 s20, 0xf2
	v_cmp_gt_i32_e64 s[22:23], s22, v192
	s_and_b64 s[24:25], s[26:27], s[24:25]
	s_movk_i32 s18, 0xf1
	v_cmp_gt_i32_e64 s[20:21], s20, v192
	s_and_b64 s[22:23], s[24:25], s[22:23]
	s_movk_i32 s16, 0xf0
	v_cmp_gt_i32_e64 s[18:19], s18, v192
	s_and_b64 s[20:21], s[22:23], s[20:21]
	s_movk_i32 s14, 0xeb
	v_cmp_gt_i32_e64 s[16:17], s16, v192
	s_and_b64 s[18:19], s[20:21], s[18:19]
	s_movk_i32 s12, 0xea
	v_cmp_gt_i32_e64 s[14:15], s14, v192
	s_and_b64 s[16:17], s[18:19], s[16:17]
	s_movk_i32 s10, 0xe9
	v_cmp_gt_i32_e64 s[12:13], s12, v192
	s_and_b64 s[14:15], s[16:17], s[14:15]
	s_movk_i32 s8, 0xe8
	v_cmp_gt_i32_e64 s[10:11], s10, v192
	s_and_b64 s[12:13], s[14:15], s[12:13]
	s_movk_i32 s6, 0xe3
	v_cmp_gt_i32_e64 s[8:9], s8, v192
	s_and_b64 s[10:11], s[12:13], s[10:11]
	s_movk_i32 s4, 0xe2
	v_cmp_gt_i32_e64 s[6:7], s6, v192
	s_and_b64 s[8:9], s[10:11], s[8:9]
	s_movk_i32 s2, 0xe1
	v_cmp_gt_i32_e64 s[4:5], s4, v192
	s_and_b64 s[6:7], s[8:9], s[6:7]
	v_cmp_gt_i32_e64 s[2:3], s2, v192
	s_and_b64 s[4:5], s[6:7], s[4:5]
	s_and_b64 s[2:3], s[4:5], s[2:3]
	s_and_b64 vcc, s[2:3], vcc
	v_cndmask_b32_e64 v108, v108, v210, s[52:53]
	v_cndmask_b32_e64 v107, v107, v210, s[50:51]
	v_cndmask_b32_e64 v106, v106, v210, s[48:49]
	v_cndmask_b32_e64 v105, v105, v210, s[46:47]
	v_cndmask_b32_e64 v104, v104, v210, s[44:45]
	v_cndmask_b32_e64 v103, v103, v210, s[42:43]
	v_cndmask_b32_e64 v102, v102, v210, s[40:41]
	v_cndmask_b32_e64 v101, v101, v210, s[38:39]
	v_cndmask_b32_e64 v100, v100, v210, s[36:37]
	v_cndmask_b32_e64 v99, v99, v210, s[34:35]
	v_cndmask_b32_e64 v98, v98, v210, s[30:31]
	v_cndmask_b32_e64 v97, v97, v210, s[28:29]
	v_cndmask_b32_e64 v125, v125, v210, s[26:27]
	v_cndmask_b32_e64 v124, v124, v210, s[24:25]
	v_cndmask_b32_e64 v123, v123, v210, s[22:23]
	v_cndmask_b32_e64 v122, v122, v210, s[20:21]
	v_cndmask_b32_e64 v121, v121, v210, s[18:19]
	v_cndmask_b32_e64 v120, v120, v210, s[16:17]
	v_cndmask_b32_e64 v119, v119, v210, s[14:15]
	v_cndmask_b32_e64 v118, v118, v210, s[12:13]
	v_cndmask_b32_e64 v117, v117, v210, s[10:11]
	v_cndmask_b32_e64 v116, v116, v210, s[8:9]
	v_cndmask_b32_e64 v115, v115, v210, s[6:7]
	v_cndmask_b32_e64 v114, v114, v210, s[4:5]
	v_cndmask_b32_e64 v113, v113, v210, s[2:3]
	v_cndmask_b32_e32 v112, v112, v210, vcc
